# NA phase layers 0-2: 16 local-key loads issued as one batch ahead of ctx-key loads instead of 8 serialized load/wait/MFMA blocks
# baseline (speedup 1.0000x reference)
.LBB0_423:
	v_or_b32_e32 v80, s70, v82
	v_mov_b64_e32 v[2:3], s[2:3]
	v_mad_i64_i32 v[2:3], s[48:49], v80, s86, v[2:3]
	s_lshl_b32 s50, s71, 7
	v_lshl_add_u64 v[2:3], v[2:3], 0, s[50:51]
	v_lshl_add_u64 v[2:3], v[2:3], 0, v[66:67]
	global_load_dwordx4 v[6:9], v[2:3], off offset:512
	s_nop 0
	global_load_dwordx4 v[2:5], v[2:3], off offset:576
	s_add_i32 s72, s72, s81
	v_lshl_add_u32 v11, s69, 11, v71
	v_cndmask_b32_e64 v10, 0, 1, s[58:59]
	s_lshl_b32 s62, s71, 6
	v_cmp_ne_u32_e64 s[48:49], 1, v10
	v_lshl_add_u32 v10, s72, 6, v11
	s_mov_b64 s[60:61], 0
	v_mov_b32_e32 v34, 0
	v_mov_b32_e32 v35, 0
	v_mov_b32_e32 v36, 0
	v_mov_b32_e32 v37, 0
	v_mov_b32_e32 v38, 0
	v_mov_b32_e32 v39, 0
	v_mov_b32_e32 v40, 0
	v_mov_b32_e32 v41, 0
	v_mov_b32_e32 v42, 0
	v_mov_b32_e32 v43, 0
	v_mov_b32_e32 v44, 0
	v_mov_b32_e32 v45, 0
	v_mov_b32_e32 v46, 0
	v_mov_b32_e32 v47, 0
	v_mov_b32_e32 v48, 0
	v_mov_b32_e32 v49, 0
	v_mov_b32_e32 v50, 0
	v_mov_b32_e32 v51, 0
	v_mov_b32_e32 v52, 0
	v_mov_b32_e32 v53, 0
	v_mov_b32_e32 v54, 0
	v_mov_b32_e32 v55, 0
	v_mov_b32_e32 v56, 0
	v_mov_b32_e32 v57, 0
	v_mov_b32_e32 v58, 0
	v_mov_b32_e32 v59, 0
	v_mov_b32_e32 v60, 0
	v_mov_b32_e32 v61, 0
	v_mov_b32_e32 v62, 0
	v_mov_b32_e32 v63, 0
	v_mov_b32_e32 v64, 0
	v_mov_b32_e32 v65, 0
	s_andn2_b64 vcc, exec, s[58:59]
	s_cbranch_vccnz .LBB0_439
	v_mov_b64_e32 v[12:13], s[2:3]
	v_mad_i64_i32 v[12:13], s[64:65], v10, s86, v[12:13]
	s_lshl_b32 s50, s62, 1
	v_lshl_add_u64 v[12:13], v[12:13], 0, s[50:51]
	v_lshl_add_u64 v[12:13], v[12:13], 0, v[66:67]
	v_add_co_u32_e32 v14, vcc, 0x30000, v12
	v_addc_co_u32_e32 v15, vcc, 0, v13, vcc
	v_add_co_u32_e32 v16, vcc, 0xc0000, v12
	v_addc_co_u32_e32 v17, vcc, 0, v13, vcc
	v_add_co_u32_e32 v18, vcc, 0xf0000, v12
	v_addc_co_u32_e32 v19, vcc, 0, v13, vcc
	v_add_co_u32_e32 v20, vcc, 0x180000, v12
	v_addc_co_u32_e32 v21, vcc, 0, v13, vcc
	v_add_co_u32_e32 v22, vcc, 0x1b0000, v12
	v_addc_co_u32_e32 v23, vcc, 0, v13, vcc
	v_add_co_u32_e32 v24, vcc, 0x240000, v12
	v_addc_co_u32_e32 v25, vcc, 0, v13, vcc
	v_add_co_u32_e32 v26, vcc, 0x270000, v12
	v_addc_co_u32_e32 v27, vcc, 0, v13, vcc
	global_load_dwordx4 v[160:163], v[12:13], off offset:1024
	global_load_dwordx4 v[164:167], v[14:15], off offset:1024
	global_load_dwordx4 v[168:171], v[16:17], off offset:1024
	global_load_dwordx4 v[172:175], v[18:19], off offset:1024
	global_load_dwordx4 v[176:179], v[20:21], off offset:1024
	global_load_dwordx4 v[180:183], v[22:23], off offset:1024
	global_load_dwordx4 v[184:187], v[24:25], off offset:1024
	global_load_dwordx4 v[188:191], v[26:27], off offset:1024
	global_load_dwordx4 v[192:195], v[12:13], off offset:1088
	global_load_dwordx4 v[196:199], v[14:15], off offset:1088
	global_load_dwordx4 v[200:203], v[16:17], off offset:1088
	global_load_dwordx4 v[204:207], v[18:19], off offset:1088
	global_load_dwordx4 v[208:211], v[20:21], off offset:1088
	global_load_dwordx4 v[214:217], v[22:23], off offset:1088
	global_load_dwordx4 v[218:221], v[24:25], off offset:1088
	global_load_dwordx4 v[222:225], v[26:27], off offset:1088
	s_and_b64 s[60:61], s[56:57], exec
.LBB0_439:
	v_lshl_add_u32 v79, s69, 8, v69
	s_nop 4
	v_add_u32_e32 v10, 0x80, v79
	v_mov_b64_e32 v[112:113], s[2:3]
	v_add_u32_e32 v14, 0x90, v79
	v_add_u32_e32 v18, 0xa0, v79
	v_add_u32_e32 v22, 0xb0, v79
	v_add_u32_e32 v26, 0xc0, v79
	v_add_u32_e32 v30, 0xd0, v79
	v_add_u32_e32 v81, 0xe0, v79
	v_mad_i64_i32 v[10:11], s[64:65], v10, s86, v[112:113]
	s_lshl_b32 s50, s62, 1
	v_mad_i64_i32 v[14:15], s[62:63], v14, s86, v[112:113]
	v_mad_i64_i32 v[18:19], s[62:63], v18, s86, v[112:113]
	v_mad_i64_i32 v[22:23], s[62:63], v22, s86, v[112:113]
	v_mad_i64_i32 v[26:27], s[62:63], v26, s86, v[112:113]
	v_mad_i64_i32 v[30:31], s[62:63], v30, s86, v[112:113]
	v_mad_i64_i32 v[108:109], s[62:63], v81, s86, v[112:113]
	v_lshl_add_u64 v[10:11], v[10:11], 0, s[50:51]
	v_lshl_add_u64 v[14:15], v[14:15], 0, s[50:51]
	v_lshl_add_u64 v[18:19], v[18:19], 0, s[50:51]
	v_lshl_add_u64 v[22:23], v[22:23], 0, s[50:51]
	v_lshl_add_u64 v[26:27], v[26:27], 0, s[50:51]
	v_lshl_add_u64 v[30:31], v[30:31], 0, s[50:51]
	v_lshl_add_u64 v[108:109], v[108:109], 0, s[50:51]
	v_lshl_add_u64 v[116:117], v[10:11], 0, v[66:67]
	v_lshl_add_u64 v[120:121], v[14:15], 0, v[66:67]
	v_lshl_add_u64 v[124:125], v[18:19], 0, v[66:67]
	v_lshl_add_u64 v[128:129], v[22:23], 0, v[66:67]
	v_lshl_add_u64 v[136:137], v[26:27], 0, v[66:67]
	v_lshl_add_u64 v[144:145], v[30:31], 0, v[66:67]
	v_lshl_add_u64 v[152:153], v[108:109], 0, v[66:67]
	global_load_dwordx4 v[10:13], v[116:117], off offset:1024
	global_load_dwordx4 v[14:17], v[120:121], off offset:1024
	global_load_dwordx4 v[18:21], v[124:125], off offset:1024
	global_load_dwordx4 v[22:25], v[128:129], off offset:1024
	global_load_dwordx4 v[26:29], v[136:137], off offset:1024
	global_load_dwordx4 v[30:33], v[144:145], off offset:1024
	global_load_dwordx4 v[108:111], v[152:153], off offset:1024
	v_add_u32_e32 v79, 0xf0, v79
	v_mad_i64_i32 v[112:113], s[62:63], v79, s86, v[112:113]
	v_lshl_add_u64 v[112:113], v[112:113], 0, s[50:51]
	v_lshl_add_u64 v[156:157], v[112:113], 0, v[66:67]
	global_load_dwordx4 v[112:115], v[156:157], off offset:1024
	s_nop 0
	global_load_dwordx4 v[116:119], v[116:117], off offset:1088
	s_sub_i32 s62, s72, s68
	global_load_dwordx4 v[120:123], v[120:121], off offset:1088
	s_mul_i32 s62, s62, 31
	global_load_dwordx4 v[124:127], v[124:125], off offset:1088
	v_mov_b32_e32 v79, 0xf149f2ca
	global_load_dwordx4 v[128:131], v[128:129], off offset:1088
	v_mov_b32_e32 v81, 0xf149f2ca
	global_load_dwordx4 v[136:139], v[136:137], off offset:1088
	s_waitcnt vmcnt(5)
	v_mfma_f32_16x16x32_f16 v[112:115], v[112:115], v[6:9], 0
	global_load_dwordx4 v[144:147], v[144:145], off offset:1088
	s_nop 0
	global_load_dwordx4 v[152:155], v[152:153], off offset:1088
	v_mfma_f32_16x16x32_f16 v[10:13], v[10:13], v[6:9], 0
	global_load_dwordx4 v[156:159], v[156:157], off offset:1088
	s_waitcnt lgkmcnt(0)
	s_barrier
	v_mfma_f32_16x16x32_f16 v[14:17], v[14:17], v[6:9], 0
	v_mfma_f32_16x16x32_f16 v[18:21], v[18:21], v[6:9], 0
	v_mfma_f32_16x16x32_f16 v[132:135], v[22:25], v[6:9], 0
	v_mfma_f32_16x16x32_f16 v[140:143], v[26:29], v[6:9], 0
	v_mfma_f32_16x16x32_f16 v[148:151], v[30:33], v[6:9], 0
	v_mfma_f32_16x16x32_f16 v[108:111], v[108:111], v[6:9], 0
	s_andn2_b64 vcc, exec, s[58:59]
	s_cbranch_vccnz .Lnakl0_skip
	v_mfma_f32_16x16x32_f16 v[160:163], v[160:163], v[6:9], 0
	v_mfma_f32_16x16x32_f16 v[164:167], v[164:167], v[6:9], 0
	v_mfma_f32_16x16x32_f16 v[168:171], v[168:171], v[6:9], 0
	v_mfma_f32_16x16x32_f16 v[172:175], v[172:175], v[6:9], 0
	v_mfma_f32_16x16x32_f16 v[176:179], v[176:179], v[6:9], 0
	v_mfma_f32_16x16x32_f16 v[180:183], v[180:183], v[6:9], 0
	v_mfma_f32_16x16x32_f16 v[184:187], v[184:187], v[6:9], 0
	v_mfma_f32_16x16x32_f16 v[188:191], v[188:191], v[6:9], 0
	v_mfma_f32_16x16x32_f16 v[62:65], v[192:195], v[2:5], v[160:163]
	v_mfma_f32_16x16x32_f16 v[54:57], v[196:199], v[2:5], v[164:167]
	v_mfma_f32_16x16x32_f16 v[58:61], v[200:203], v[2:5], v[168:171]
	v_mfma_f32_16x16x32_f16 v[46:49], v[204:207], v[2:5], v[172:175]
	v_mfma_f32_16x16x32_f16 v[50:53], v[208:211], v[2:5], v[176:179]
	v_mfma_f32_16x16x32_f16 v[38:41], v[214:217], v[2:5], v[180:183]
	v_mfma_f32_16x16x32_f16 v[42:45], v[218:221], v[2:5], v[184:187]
	v_mfma_f32_16x16x32_f16 v[34:37], v[222:225], v[2:5], v[188:191]
.Lnakl0_skip:
	s_waitcnt vmcnt(7)
	v_mfma_f32_16x16x32_f16 v[30:33], v[116:119], v[2:5], v[10:13]
	s_waitcnt vmcnt(6)
	v_mfma_f32_16x16x32_f16 v[26:29], v[120:123], v[2:5], v[14:17]
	s_waitcnt vmcnt(5)
	v_mfma_f32_16x16x32_f16 v[22:25], v[124:127], v[2:5], v[18:21]
	s_waitcnt vmcnt(4)
	v_mfma_f32_16x16x32_f16 v[18:21], v[128:131], v[2:5], v[132:135]
	s_waitcnt vmcnt(3)
	v_mfma_f32_16x16x32_f16 v[14:17], v[136:139], v[2:5], v[140:143]
	s_waitcnt vmcnt(2)
	v_mfma_f32_16x16x32_f16 v[10:13], v[144:147], v[2:5], v[148:151]
	s_waitcnt vmcnt(1)
	v_mfma_f32_16x16x32_f16 v[6:9], v[152:155], v[2:5], v[108:111]
	s_waitcnt vmcnt(0)
	v_mfma_f32_16x16x32_f16 v[2:5], v[156:159], v[2:5], v[112:115]
	s_nop 2
	v_sub_u32_e32 v115, s62, v82
	v_lshl_add_u32 v108, v115, 2, v86
	s_and_saveexec_b64 s[62:63], s[60:61]
	s_cbranch_execz .LBB0_441
	ds_read_b32 v81, v108 offset:928
	s_waitcnt lgkmcnt(0)
	v_add_f32_e32 v81, v62, v81
